# indexer pass C2: tie budget kept as thr minus remaining so the effective threshold is one med3; 4th-group last-key block predicated
# speedup vs baseline: 1.0041x; 1.0023x over previous
.LBB0_708:
	s_or_b64 exec, exec, s[0:1]
	v_add_u32_e32 v15, v16, v15
	v_sub_u32_sdwa v13, v15, v13 dst_sel:DWORD dst_unused:UNUSED_PAD src0_sel:WORD_0 src1_sel:DWORD
	v_sub_u32_sdwa v15, v15, v14 dst_sel:DWORD dst_unused:UNUSED_PAD src0_sel:WORD_1 src1_sel:DWORD
	v_add_u32_e32 v4, v13, v4
	v_add_u32_e32 v5, v15, v5
	v_lshl_or_b32 v14, v15, 16, v13
	v_lshl_or_b32 v15, v5, 16, v4
	v_add_u32_e32 v4, v4, v6
	v_add_u32_e32 v5, v5, v7
	v_lshl_or_b32 v16, v5, 16, v4
	v_add_u32_e32 v4, v4, v8
	v_add_u32_e32 v5, v5, v9
	v_lshl_or_b32 v17, v5, 16, v4
	s_and_b64 vcc, exec, s[16:17]
	ds_write_b128 v247, v[14:17] offset:3072
	s_waitcnt lgkmcnt(0)
	s_barrier
	s_cbranch_vccz .LBB0_358
	v_lshl_add_u64 v[4:5], s[94:95], 0, v[10:11]
	v_readlane_b32 s0, v255, 4
	ds_read2_b32 v[36:37], v12 offset0:64 offset1:96
	v_lshlrev_b64 v[4:5], 9, v[4:5]
	v_readlane_b32 s1, v255, 5
	v_lshlrev_b32_e32 v40, 4, v2
	v_mov_b32_e32 v41, v3
	v_lshl_add_u64 v[38:39], s[0:1], 0, v[4:5]
	v_readlane_b32 s0, v255, 19
	v_lshlrev_b32_e32 v4, 5, v10
	v_ashrrev_i32_e32 v5, 31, v4
	v_lshl_add_u32 v49, v10, 10, s0
	v_readlane_b32 s0, v255, 20
	v_readlane_b32 s1, v255, 21
	v_cmp_eq_u32_e64 s[22:23], 0, v2
	s_mov_b64 s[16:17], s[66:67]
	v_lshl_add_u64 v[42:43], s[0:1], 0, v[4:5]
	s_mov_b32 s36, s58
	s_mov_b64 s[40:41], 0x2000
	s_mov_b64 s[42:43], 0x8000
	s_waitcnt lgkmcnt(0)
	v_add_u32_e32 v52, -1, v36
	v_sub_u32_e32 v53, v36, v37
	s_branch .LBB0_712

.LBB0_718:
	v_lshl_add_u64 v[8:9], v[6:7], 1, s[12:13]
	global_load_dwordx4 v[4:7], v[8:9], off offset:16
	s_nop 0
	global_load_dwordx4 v[8:11], v[8:9], off
	s_and_saveexec_b64 s[24:25], vcc
	s_cbranch_execz .LBB0_845
	ds_read_u16 v2, v49 offset:36864
	v_add_u32_e32 v44, 0x11200, v49
	ds_read_b32 v44, v44
	s_waitcnt vmcnt(6)
	s_waitcnt lgkmcnt(1)
	v_lshrrev_b32_e32 v45, 8, v2
	v_and_b32_e32 v2, 0xff, v2
	v_cndmask_b32_e64 v45, v45, 0, s[22:23]
	v_cndmask_b32_e64 v2, v2, 0, s[22:23]
	s_waitcnt lgkmcnt(0)
	v_add_u32_sdwa v51, v45, v44 dst_sel:DWORD dst_unused:UNUSED_PAD src0_sel:DWORD src1_sel:WORD_1
	v_add_u32_sdwa v214, v2, v44 dst_sel:DWORD dst_unused:UNUSED_PAD src0_sel:DWORD src1_sel:WORD_0
	v_lshl_add_u64 v[44:45], v[40:41], 0, s[16:17]
	v_min_i32_e32 v2, v51, v37
	v_add_u32_e32 v2, v2, v214
	v_add_u32_e32 v51, v53, v51
	v_med3_i32 v214, v51, v52, v36
	v_cmp_gt_i32_sdwa s[0:1], v32, v214 src0_sel:WORD_0 src1_sel:DWORD
	v_cmp_eq_u32_sdwa s[30:31], v32, v36 src0_sel:WORD_0 src1_sel:DWORD
	v_lshl_add_u64 v[46:47], v[2:3], 1, v[38:39]
	s_and_saveexec_b64 s[34:35], s[0:1]
	global_store_short v[46:47], v44, off
	s_mov_b64 exec, s[34:35]
	v_addc_co_u32_e64 v2, vcc, 0, v2, s[0:1]
	v_addc_co_u32_e64 v51, vcc, 0, v51, s[30:31]
	v_lshl_add_u64 v[46:47], v[44:45], 0, 1
	v_med3_i32 v214, v51, v52, v36
	v_cmp_gt_i32_sdwa s[0:1], v32, v214 src0_sel:WORD_1 src1_sel:DWORD
	v_cmp_eq_u32_sdwa s[30:31], v32, v36 src0_sel:WORD_1 src1_sel:DWORD
	v_lshl_add_u64 v[212:213], v[2:3], 1, v[38:39]
	s_and_saveexec_b64 s[34:35], s[0:1]
	global_store_short v[212:213], v46, off
	s_mov_b64 exec, s[34:35]
	v_addc_co_u32_e64 v2, vcc, 0, v2, s[0:1]
	v_addc_co_u32_e64 v51, vcc, 0, v51, s[30:31]
	v_lshl_add_u64 v[46:47], v[44:45], 0, 2
	v_med3_i32 v214, v51, v52, v36
	v_cmp_gt_i32_sdwa s[0:1], v33, v214 src0_sel:WORD_0 src1_sel:DWORD
	v_cmp_eq_u32_sdwa s[30:31], v33, v36 src0_sel:WORD_0 src1_sel:DWORD
	v_lshl_add_u64 v[212:213], v[2:3], 1, v[38:39]
	s_and_saveexec_b64 s[34:35], s[0:1]
	global_store_short v[212:213], v46, off
	s_mov_b64 exec, s[34:35]
	v_addc_co_u32_e64 v2, vcc, 0, v2, s[0:1]
	v_addc_co_u32_e64 v51, vcc, 0, v51, s[30:31]
	v_lshl_add_u64 v[46:47], v[44:45], 0, 3
	v_med3_i32 v214, v51, v52, v36
	v_cmp_gt_i32_sdwa s[0:1], v33, v214 src0_sel:WORD_1 src1_sel:DWORD
	v_cmp_eq_u32_sdwa s[30:31], v33, v36 src0_sel:WORD_1 src1_sel:DWORD
	v_lshl_add_u64 v[32:33], v[2:3], 1, v[38:39]
	s_and_saveexec_b64 s[34:35], s[0:1]
	global_store_short v[32:33], v46, off
	s_mov_b64 exec, s[34:35]
	v_addc_co_u32_e64 v2, vcc, 0, v2, s[0:1]
	v_addc_co_u32_e64 v51, vcc, 0, v51, s[30:31]
	v_lshl_add_u64 v[32:33], v[44:45], 0, 4
	v_med3_i32 v214, v51, v52, v36
	v_cmp_gt_i32_sdwa s[0:1], v34, v214 src0_sel:WORD_0 src1_sel:DWORD
	v_cmp_eq_u32_sdwa s[30:31], v34, v36 src0_sel:WORD_0 src1_sel:DWORD
	v_lshl_add_u64 v[46:47], v[2:3], 1, v[38:39]
	s_and_saveexec_b64 s[34:35], s[0:1]
	global_store_short v[46:47], v32, off
	s_mov_b64 exec, s[34:35]
	v_addc_co_u32_e64 v2, vcc, 0, v2, s[0:1]
	v_addc_co_u32_e64 v51, vcc, 0, v51, s[30:31]
	v_lshl_add_u64 v[32:33], v[44:45], 0, 5
	v_med3_i32 v214, v51, v52, v36
	v_cmp_gt_i32_sdwa s[0:1], v34, v214 src0_sel:WORD_1 src1_sel:DWORD
	v_cmp_eq_u32_sdwa s[30:31], v34, v36 src0_sel:WORD_1 src1_sel:DWORD
	v_lshl_add_u64 v[46:47], v[2:3], 1, v[38:39]
	s_and_saveexec_b64 s[34:35], s[0:1]
	global_store_short v[46:47], v32, off
	s_mov_b64 exec, s[34:35]
	v_addc_co_u32_e64 v2, vcc, 0, v2, s[0:1]
	v_addc_co_u32_e64 v51, vcc, 0, v51, s[30:31]
	v_lshl_add_u64 v[32:33], v[44:45], 0, 6
	v_med3_i32 v214, v51, v52, v36
	v_cmp_gt_i32_sdwa s[0:1], v35, v214 src0_sel:WORD_0 src1_sel:DWORD
	v_cmp_eq_u32_sdwa s[30:31], v35, v36 src0_sel:WORD_0 src1_sel:DWORD
	v_lshl_add_u64 v[46:47], v[2:3], 1, v[38:39]
	s_and_saveexec_b64 s[34:35], s[0:1]
	global_store_short v[46:47], v32, off
	s_mov_b64 exec, s[34:35]
	v_addc_co_u32_e64 v2, vcc, 0, v2, s[0:1]
	v_addc_co_u32_e64 v51, vcc, 0, v51, s[30:31]
	v_lshl_add_u64 v[32:33], v[44:45], 0, 7
	v_med3_i32 v214, v51, v52, v36
	v_cmp_gt_i32_sdwa s[0:1], v35, v214 src0_sel:WORD_1 src1_sel:DWORD
	v_cmp_eq_u32_sdwa s[30:31], v35, v36 src0_sel:WORD_1 src1_sel:DWORD
	v_lshl_add_u64 v[34:35], v[2:3], 1, v[38:39]
	s_and_saveexec_b64 s[34:35], s[0:1]
	global_store_short v[34:35], v32, off
	s_mov_b64 exec, s[34:35]
	v_addc_co_u32_e64 v2, vcc, 0, v2, s[0:1]
	v_addc_co_u32_e64 v51, vcc, 0, v51, s[30:31]
	v_lshl_add_u64 v[32:33], v[44:45], 0, 8
	v_med3_i32 v214, v51, v52, v36
	v_cmp_gt_i32_sdwa s[0:1], v28, v214 src0_sel:WORD_0 src1_sel:DWORD
	v_cmp_eq_u32_sdwa s[30:31], v28, v36 src0_sel:WORD_0 src1_sel:DWORD
	v_lshl_add_u64 v[34:35], v[2:3], 1, v[38:39]
	s_and_saveexec_b64 s[34:35], s[0:1]
	global_store_short v[34:35], v32, off
	s_mov_b64 exec, s[34:35]
	v_addc_co_u32_e64 v2, vcc, 0, v2, s[0:1]
	v_addc_co_u32_e64 v51, vcc, 0, v51, s[30:31]
	v_lshl_add_u64 v[32:33], v[44:45], 0, 9
	v_med3_i32 v214, v51, v52, v36
	v_cmp_gt_i32_sdwa s[0:1], v28, v214 src0_sel:WORD_1 src1_sel:DWORD
	v_cmp_eq_u32_sdwa s[30:31], v28, v36 src0_sel:WORD_1 src1_sel:DWORD
	v_lshl_add_u64 v[34:35], v[2:3], 1, v[38:39]
	s_and_saveexec_b64 s[34:35], s[0:1]
	global_store_short v[34:35], v32, off
	s_mov_b64 exec, s[34:35]
	v_addc_co_u32_e64 v2, vcc, 0, v2, s[0:1]
	v_addc_co_u32_e64 v51, vcc, 0, v51, s[30:31]
	v_lshl_add_u64 v[32:33], v[44:45], 0, 10
	v_med3_i32 v214, v51, v52, v36
	v_cmp_gt_i32_sdwa s[0:1], v29, v214 src0_sel:WORD_0 src1_sel:DWORD
	v_cmp_eq_u32_sdwa s[30:31], v29, v36 src0_sel:WORD_0 src1_sel:DWORD
	v_lshl_add_u64 v[34:35], v[2:3], 1, v[38:39]
	s_and_saveexec_b64 s[34:35], s[0:1]
	global_store_short v[34:35], v32, off
	s_mov_b64 exec, s[34:35]
	v_addc_co_u32_e64 v2, vcc, 0, v2, s[0:1]
	v_addc_co_u32_e64 v51, vcc, 0, v51, s[30:31]
	v_lshl_add_u64 v[32:33], v[44:45], 0, 11
	v_med3_i32 v214, v51, v52, v36
	v_cmp_gt_i32_sdwa s[0:1], v29, v214 src0_sel:WORD_1 src1_sel:DWORD
	v_cmp_eq_u32_sdwa s[30:31], v29, v36 src0_sel:WORD_1 src1_sel:DWORD
	v_lshl_add_u64 v[28:29], v[2:3], 1, v[38:39]
	s_and_saveexec_b64 s[34:35], s[0:1]
	global_store_short v[28:29], v32, off
	s_mov_b64 exec, s[34:35]
	v_addc_co_u32_e64 v2, vcc, 0, v2, s[0:1]
	v_addc_co_u32_e64 v51, vcc, 0, v51, s[30:31]
	v_lshl_add_u64 v[28:29], v[44:45], 0, 12
	v_med3_i32 v214, v51, v52, v36
	v_cmp_gt_i32_sdwa s[0:1], v30, v214 src0_sel:WORD_0 src1_sel:DWORD
	v_cmp_eq_u32_sdwa s[30:31], v30, v36 src0_sel:WORD_0 src1_sel:DWORD
	v_lshl_add_u64 v[32:33], v[2:3], 1, v[38:39]
	s_and_saveexec_b64 s[34:35], s[0:1]
	global_store_short v[32:33], v28, off
	s_mov_b64 exec, s[34:35]
	v_addc_co_u32_e64 v2, vcc, 0, v2, s[0:1]
	v_addc_co_u32_e64 v51, vcc, 0, v51, s[30:31]
	v_lshl_add_u64 v[28:29], v[44:45], 0, 13
	v_med3_i32 v214, v51, v52, v36
	v_cmp_gt_i32_sdwa s[0:1], v30, v214 src0_sel:WORD_1 src1_sel:DWORD
	v_cmp_eq_u32_sdwa s[30:31], v30, v36 src0_sel:WORD_1 src1_sel:DWORD
	v_lshl_add_u64 v[32:33], v[2:3], 1, v[38:39]
	s_and_saveexec_b64 s[34:35], s[0:1]
	global_store_short v[32:33], v28, off
	s_mov_b64 exec, s[34:35]
	v_addc_co_u32_e64 v2, vcc, 0, v2, s[0:1]
	v_addc_co_u32_e64 v51, vcc, 0, v51, s[30:31]
	v_lshl_add_u64 v[28:29], v[44:45], 0, 14
	v_med3_i32 v214, v51, v52, v36
	v_cmp_gt_i32_sdwa s[0:1], v31, v214 src0_sel:WORD_0 src1_sel:DWORD
	v_cmp_eq_u32_sdwa s[30:31], v31, v36 src0_sel:WORD_0 src1_sel:DWORD
	v_lshl_add_u64 v[32:33], v[2:3], 1, v[38:39]
	s_and_saveexec_b64 s[34:35], s[0:1]
	global_store_short v[32:33], v28, off
	s_mov_b64 exec, s[34:35]
	v_addc_co_u32_e64 v2, vcc, 0, v2, s[0:1]
	v_addc_co_u32_e64 v51, vcc, 0, v51, s[30:31]
	v_med3_i32 v214, v51, v52, v36
	v_cmp_gt_i32_sdwa s[30:31], v31, v214 src0_sel:WORD_1 src1_sel:DWORD
	v_lshl_add_u64 v[28:29], v[2:3], 1, v[38:39]
	v_or_b32_e32 v214, 15, v44
	s_and_saveexec_b64 s[34:35], s[30:31]
	global_store_short v[28:29], v214, off
	s_mov_b64 exec, s[34:35]
.LBB0_843:
.LBB0_844:
.LBB0_845:
	s_or_b64 exec, exec, s[24:25]
	s_andn2_b64 vcc, exec, s[18:19]
	s_cbranch_vccnz .LBB0_975
	ds_read_u16 v2, v50 offset:36896
	s_waitcnt lgkmcnt(0)
	v_cmp_ne_u16_e32 vcc, 0, v2
	s_and_saveexec_b64 s[18:19], vcc
	s_cbranch_execz .LBB0_973
	ds_read_u16 v2, v49 offset:36896
	s_waitcnt vmcnt(7)
	v_add_u32_e32 v28, 0x11220, v49
	ds_read_b32 v28, v28
	v_lshl_add_u64 v[30:31], v[40:41], 0, s[16:17]
	s_waitcnt vmcnt(4)
	s_waitcnt lgkmcnt(1)
	v_lshrrev_b32_e32 v29, 8, v2
	v_and_b32_e32 v2, 0xff, v2
	v_cndmask_b32_e64 v29, v29, 0, s[22:23]
	v_cndmask_b32_e64 v2, v2, 0, s[22:23]
	s_waitcnt lgkmcnt(0)
	v_add_u32_sdwa v34, v29, v28 dst_sel:DWORD dst_unused:UNUSED_PAD src0_sel:DWORD src1_sel:WORD_1
	v_add_u32_sdwa v35, v2, v28 dst_sel:DWORD dst_unused:UNUSED_PAD src0_sel:DWORD src1_sel:WORD_0
	v_lshl_add_u64 v[28:29], v[30:31], 0, s[84:85]
	v_min_i32_e32 v2, v34, v37
	v_add_u32_e32 v2, v2, v35
	v_add_u32_e32 v34, v53, v34
	v_med3_i32 v35, v34, v52, v36
	v_cmp_gt_i32_sdwa s[0:1], v24, v35 src0_sel:WORD_0 src1_sel:DWORD
	v_cmp_eq_u32_sdwa s[24:25], v24, v36 src0_sel:WORD_0 src1_sel:DWORD
	v_lshl_add_u64 v[32:33], v[2:3], 1, v[38:39]
	s_and_saveexec_b64 s[30:31], s[0:1]
	global_store_short v[32:33], v28, off
	s_mov_b64 exec, s[30:31]
	v_addc_co_u32_e64 v2, vcc, 0, v2, s[0:1]
	v_addc_co_u32_e64 v34, vcc, 0, v34, s[24:25]
	v_add_u32_e32 v32, 0x101, v30
	v_med3_i32 v35, v34, v52, v36
	v_cmp_gt_i32_sdwa s[0:1], v24, v35 src0_sel:WORD_1 src1_sel:DWORD
	v_cmp_eq_u32_sdwa s[24:25], v24, v36 src0_sel:WORD_1 src1_sel:DWORD
	v_lshl_add_u64 v[44:45], v[2:3], 1, v[38:39]
	s_and_saveexec_b64 s[30:31], s[0:1]
	global_store_short v[44:45], v32, off
	s_mov_b64 exec, s[30:31]
	v_addc_co_u32_e64 v2, vcc, 0, v2, s[0:1]
	v_addc_co_u32_e64 v34, vcc, 0, v34, s[24:25]
	v_add_u32_e32 v32, 0x102, v30
	v_med3_i32 v35, v34, v52, v36
	v_cmp_gt_i32_sdwa s[0:1], v25, v35 src0_sel:WORD_0 src1_sel:DWORD
	v_cmp_eq_u32_sdwa s[24:25], v25, v36 src0_sel:WORD_0 src1_sel:DWORD
	v_lshl_add_u64 v[44:45], v[2:3], 1, v[38:39]
	s_and_saveexec_b64 s[30:31], s[0:1]
	global_store_short v[44:45], v32, off
	s_mov_b64 exec, s[30:31]
	v_addc_co_u32_e64 v2, vcc, 0, v2, s[0:1]
	v_addc_co_u32_e64 v34, vcc, 0, v34, s[24:25]
	v_add_u32_e32 v32, 0x103, v30
	v_med3_i32 v35, v34, v52, v36
	v_cmp_gt_i32_sdwa s[0:1], v25, v35 src0_sel:WORD_1 src1_sel:DWORD
	v_cmp_eq_u32_sdwa s[24:25], v25, v36 src0_sel:WORD_1 src1_sel:DWORD
	v_lshl_add_u64 v[24:25], v[2:3], 1, v[38:39]
	s_and_saveexec_b64 s[30:31], s[0:1]
	global_store_short v[24:25], v32, off
	s_mov_b64 exec, s[30:31]
	v_addc_co_u32_e64 v2, vcc, 0, v2, s[0:1]
	v_addc_co_u32_e64 v34, vcc, 0, v34, s[24:25]
	v_add_u32_e32 v24, 0x104, v30
	v_med3_i32 v35, v34, v52, v36
	v_cmp_gt_i32_sdwa s[0:1], v26, v35 src0_sel:WORD_0 src1_sel:DWORD
	v_cmp_eq_u32_sdwa s[24:25], v26, v36 src0_sel:WORD_0 src1_sel:DWORD
	v_lshl_add_u64 v[32:33], v[2:3], 1, v[38:39]
	s_and_saveexec_b64 s[30:31], s[0:1]
	global_store_short v[32:33], v24, off
	s_mov_b64 exec, s[30:31]
	v_addc_co_u32_e64 v2, vcc, 0, v2, s[0:1]
	v_addc_co_u32_e64 v34, vcc, 0, v34, s[24:25]
	v_add_u32_e32 v24, 0x105, v30
	v_med3_i32 v35, v34, v52, v36
	v_cmp_gt_i32_sdwa s[0:1], v26, v35 src0_sel:WORD_1 src1_sel:DWORD
	v_cmp_eq_u32_sdwa s[24:25], v26, v36 src0_sel:WORD_1 src1_sel:DWORD
	v_lshl_add_u64 v[32:33], v[2:3], 1, v[38:39]
	s_and_saveexec_b64 s[30:31], s[0:1]
	global_store_short v[32:33], v24, off
	s_mov_b64 exec, s[30:31]
	v_addc_co_u32_e64 v2, vcc, 0, v2, s[0:1]
	v_addc_co_u32_e64 v34, vcc, 0, v34, s[24:25]
	v_add_u32_e32 v24, 0x106, v30
	v_med3_i32 v35, v34, v52, v36
	v_cmp_gt_i32_sdwa s[0:1], v27, v35 src0_sel:WORD_0 src1_sel:DWORD
	v_cmp_eq_u32_sdwa s[24:25], v27, v36 src0_sel:WORD_0 src1_sel:DWORD
	v_lshl_add_u64 v[32:33], v[2:3], 1, v[38:39]
	s_and_saveexec_b64 s[30:31], s[0:1]
	global_store_short v[32:33], v24, off
	s_mov_b64 exec, s[30:31]
	v_addc_co_u32_e64 v2, vcc, 0, v2, s[0:1]
	v_addc_co_u32_e64 v34, vcc, 0, v34, s[24:25]
	v_add_u32_e32 v24, 0x107, v30
	v_med3_i32 v35, v34, v52, v36
	v_cmp_gt_i32_sdwa s[0:1], v27, v35 src0_sel:WORD_1 src1_sel:DWORD
	v_cmp_eq_u32_sdwa s[24:25], v27, v36 src0_sel:WORD_1 src1_sel:DWORD
	v_lshl_add_u64 v[26:27], v[2:3], 1, v[38:39]
	s_and_saveexec_b64 s[30:31], s[0:1]
	global_store_short v[26:27], v24, off
	s_mov_b64 exec, s[30:31]
	v_addc_co_u32_e64 v2, vcc, 0, v2, s[0:1]
	v_addc_co_u32_e64 v34, vcc, 0, v34, s[24:25]
	v_add_u32_e32 v24, 0x108, v30
	v_med3_i32 v35, v34, v52, v36
	v_cmp_gt_i32_sdwa s[0:1], v20, v35 src0_sel:WORD_0 src1_sel:DWORD
	v_cmp_eq_u32_sdwa s[24:25], v20, v36 src0_sel:WORD_0 src1_sel:DWORD
	v_lshl_add_u64 v[26:27], v[2:3], 1, v[38:39]
	s_and_saveexec_b64 s[30:31], s[0:1]
	global_store_short v[26:27], v24, off
	s_mov_b64 exec, s[30:31]
	v_addc_co_u32_e64 v2, vcc, 0, v2, s[0:1]
	v_addc_co_u32_e64 v34, vcc, 0, v34, s[24:25]
	v_add_u32_e32 v24, 0x109, v30
	v_med3_i32 v35, v34, v52, v36
	v_cmp_gt_i32_sdwa s[0:1], v20, v35 src0_sel:WORD_1 src1_sel:DWORD
	v_cmp_eq_u32_sdwa s[24:25], v20, v36 src0_sel:WORD_1 src1_sel:DWORD
	v_lshl_add_u64 v[26:27], v[2:3], 1, v[38:39]
	s_and_saveexec_b64 s[30:31], s[0:1]
	global_store_short v[26:27], v24, off
	s_mov_b64 exec, s[30:31]
	v_addc_co_u32_e64 v2, vcc, 0, v2, s[0:1]
	v_addc_co_u32_e64 v34, vcc, 0, v34, s[24:25]
	v_add_u32_e32 v24, 0x10a, v30
	v_med3_i32 v35, v34, v52, v36
	v_cmp_gt_i32_sdwa s[0:1], v21, v35 src0_sel:WORD_0 src1_sel:DWORD
	v_cmp_eq_u32_sdwa s[24:25], v21, v36 src0_sel:WORD_0 src1_sel:DWORD
	v_lshl_add_u64 v[26:27], v[2:3], 1, v[38:39]
	s_and_saveexec_b64 s[30:31], s[0:1]
	global_store_short v[26:27], v24, off
	s_mov_b64 exec, s[30:31]
	v_addc_co_u32_e64 v2, vcc, 0, v2, s[0:1]
	v_addc_co_u32_e64 v34, vcc, 0, v34, s[24:25]
	v_add_u32_e32 v24, 0x10b, v30
	v_med3_i32 v35, v34, v52, v36
	v_cmp_gt_i32_sdwa s[0:1], v21, v35 src0_sel:WORD_1 src1_sel:DWORD
	v_cmp_eq_u32_sdwa s[24:25], v21, v36 src0_sel:WORD_1 src1_sel:DWORD
	v_lshl_add_u64 v[20:21], v[2:3], 1, v[38:39]
	s_and_saveexec_b64 s[30:31], s[0:1]
	global_store_short v[20:21], v24, off
	s_mov_b64 exec, s[30:31]
	v_addc_co_u32_e64 v2, vcc, 0, v2, s[0:1]
	v_addc_co_u32_e64 v34, vcc, 0, v34, s[24:25]
	v_add_u32_e32 v20, 0x10c, v30
	v_med3_i32 v35, v34, v52, v36
	v_cmp_gt_i32_sdwa s[0:1], v22, v35 src0_sel:WORD_0 src1_sel:DWORD
	v_cmp_eq_u32_sdwa s[24:25], v22, v36 src0_sel:WORD_0 src1_sel:DWORD
	v_lshl_add_u64 v[24:25], v[2:3], 1, v[38:39]
	s_and_saveexec_b64 s[30:31], s[0:1]
	global_store_short v[24:25], v20, off
	s_mov_b64 exec, s[30:31]
	v_addc_co_u32_e64 v2, vcc, 0, v2, s[0:1]
	v_addc_co_u32_e64 v34, vcc, 0, v34, s[24:25]
	v_add_u32_e32 v20, 0x10d, v30
	v_med3_i32 v35, v34, v52, v36
	v_cmp_gt_i32_sdwa s[0:1], v22, v35 src0_sel:WORD_1 src1_sel:DWORD
	v_cmp_eq_u32_sdwa s[24:25], v22, v36 src0_sel:WORD_1 src1_sel:DWORD
	v_lshl_add_u64 v[24:25], v[2:3], 1, v[38:39]
	s_and_saveexec_b64 s[30:31], s[0:1]
	global_store_short v[24:25], v20, off
	s_mov_b64 exec, s[30:31]
	v_addc_co_u32_e64 v2, vcc, 0, v2, s[0:1]
	v_addc_co_u32_e64 v34, vcc, 0, v34, s[24:25]
	v_add_u32_e32 v20, 0x10e, v30
	v_med3_i32 v35, v34, v52, v36
	v_cmp_gt_i32_sdwa s[0:1], v23, v35 src0_sel:WORD_0 src1_sel:DWORD
	v_cmp_eq_u32_sdwa s[24:25], v23, v36 src0_sel:WORD_0 src1_sel:DWORD
	v_lshl_add_u64 v[24:25], v[2:3], 1, v[38:39]
	s_and_saveexec_b64 s[30:31], s[0:1]
	global_store_short v[24:25], v20, off
	s_mov_b64 exec, s[30:31]
	v_addc_co_u32_e64 v2, vcc, 0, v2, s[0:1]
	v_addc_co_u32_e64 v34, vcc, 0, v34, s[24:25]
	v_med3_i32 v35, v34, v52, v36
	v_cmp_gt_i32_sdwa s[24:25], v23, v35 src0_sel:WORD_1 src1_sel:DWORD
	v_lshl_add_u64 v[20:21], v[2:3], 1, v[38:39]
	v_or_b32_e32 v35, 15, v28
	s_and_saveexec_b64 s[30:31], s[24:25]
	global_store_short v[20:21], v35, off
	s_mov_b64 exec, s[30:31]

.LBB0_976:
	ds_read_u16 v2, v50 offset:36928
	s_waitcnt lgkmcnt(0)
	v_cmp_ne_u16_e32 vcc, 0, v2
	s_and_saveexec_b64 s[18:19], vcc
	s_cbranch_execz .LBB0_1103
	ds_read_u16 v2, v49 offset:36928
	s_waitcnt vmcnt(5)
	v_add_u32_e32 v20, 0x11240, v49
	ds_read_b32 v20, v20
	v_lshl_add_u64 v[22:23], v[40:41], 0, s[16:17]
	s_mov_b64 s[0:1], 0x200
	s_waitcnt lgkmcnt(1)
	v_lshrrev_b32_e32 v21, 8, v2
	v_and_b32_e32 v2, 0xff, v2
	v_cndmask_b32_e64 v21, v21, 0, s[22:23]
	v_cndmask_b32_e64 v2, v2, 0, s[22:23]
	s_waitcnt vmcnt(4) lgkmcnt(0)
	v_add_u32_sdwa v26, v21, v20 dst_sel:DWORD dst_unused:UNUSED_PAD src0_sel:DWORD src1_sel:WORD_1
	v_add_u32_sdwa v27, v2, v20 dst_sel:DWORD dst_unused:UNUSED_PAD src0_sel:DWORD src1_sel:WORD_0
	v_lshl_add_u64 v[20:21], v[22:23], 0, s[0:1]
	s_waitcnt vmcnt(2)
	v_min_i32_e32 v2, v26, v37
	v_add_u32_e32 v2, v2, v27
	v_add_u32_e32 v26, v53, v26
	v_med3_i32 v27, v26, v52, v36
	v_cmp_gt_i32_sdwa s[0:1], v16, v27 src0_sel:WORD_0 src1_sel:DWORD
	v_cmp_eq_u32_sdwa s[24:25], v16, v36 src0_sel:WORD_0 src1_sel:DWORD
	v_lshl_add_u64 v[24:25], v[2:3], 1, v[38:39]
	s_and_saveexec_b64 s[28:29], s[0:1]
	global_store_short v[24:25], v20, off
	s_mov_b64 exec, s[28:29]
	v_addc_co_u32_e64 v2, vcc, 0, v2, s[0:1]
	v_addc_co_u32_e64 v26, vcc, 0, v26, s[24:25]
	v_add_u32_e32 v24, 0x201, v22
	v_med3_i32 v27, v26, v52, v36
	v_cmp_gt_i32_sdwa s[0:1], v16, v27 src0_sel:WORD_1 src1_sel:DWORD
	v_cmp_eq_u32_sdwa s[24:25], v16, v36 src0_sel:WORD_1 src1_sel:DWORD
	v_lshl_add_u64 v[28:29], v[2:3], 1, v[38:39]
	s_and_saveexec_b64 s[28:29], s[0:1]
	global_store_short v[28:29], v24, off
	s_mov_b64 exec, s[28:29]
	v_addc_co_u32_e64 v2, vcc, 0, v2, s[0:1]
	v_addc_co_u32_e64 v26, vcc, 0, v26, s[24:25]
	v_add_u32_e32 v24, 0x202, v22
	v_med3_i32 v27, v26, v52, v36
	v_cmp_gt_i32_sdwa s[0:1], v17, v27 src0_sel:WORD_0 src1_sel:DWORD
	v_cmp_eq_u32_sdwa s[24:25], v17, v36 src0_sel:WORD_0 src1_sel:DWORD
	v_lshl_add_u64 v[28:29], v[2:3], 1, v[38:39]
	s_and_saveexec_b64 s[28:29], s[0:1]
	global_store_short v[28:29], v24, off
	s_mov_b64 exec, s[28:29]
	v_addc_co_u32_e64 v2, vcc, 0, v2, s[0:1]
	v_addc_co_u32_e64 v26, vcc, 0, v26, s[24:25]
	v_add_u32_e32 v24, 0x203, v22
	v_med3_i32 v27, v26, v52, v36
	v_cmp_gt_i32_sdwa s[0:1], v17, v27 src0_sel:WORD_1 src1_sel:DWORD
	v_cmp_eq_u32_sdwa s[24:25], v17, v36 src0_sel:WORD_1 src1_sel:DWORD
	v_lshl_add_u64 v[16:17], v[2:3], 1, v[38:39]
	s_and_saveexec_b64 s[28:29], s[0:1]
	global_store_short v[16:17], v24, off
	s_mov_b64 exec, s[28:29]
	v_addc_co_u32_e64 v2, vcc, 0, v2, s[0:1]
	v_addc_co_u32_e64 v26, vcc, 0, v26, s[24:25]
	v_add_u32_e32 v16, 0x204, v22
	v_med3_i32 v27, v26, v52, v36
	v_cmp_gt_i32_sdwa s[0:1], v18, v27 src0_sel:WORD_0 src1_sel:DWORD
	v_cmp_eq_u32_sdwa s[24:25], v18, v36 src0_sel:WORD_0 src1_sel:DWORD
	v_lshl_add_u64 v[24:25], v[2:3], 1, v[38:39]
	s_and_saveexec_b64 s[28:29], s[0:1]
	global_store_short v[24:25], v16, off
	s_mov_b64 exec, s[28:29]
	v_addc_co_u32_e64 v2, vcc, 0, v2, s[0:1]
	v_addc_co_u32_e64 v26, vcc, 0, v26, s[24:25]
	v_add_u32_e32 v16, 0x205, v22
	v_med3_i32 v27, v26, v52, v36
	v_cmp_gt_i32_sdwa s[0:1], v18, v27 src0_sel:WORD_1 src1_sel:DWORD
	v_cmp_eq_u32_sdwa s[24:25], v18, v36 src0_sel:WORD_1 src1_sel:DWORD
	v_lshl_add_u64 v[24:25], v[2:3], 1, v[38:39]
	s_and_saveexec_b64 s[28:29], s[0:1]
	global_store_short v[24:25], v16, off
	s_mov_b64 exec, s[28:29]
	v_addc_co_u32_e64 v2, vcc, 0, v2, s[0:1]
	v_addc_co_u32_e64 v26, vcc, 0, v26, s[24:25]
	v_add_u32_e32 v16, 0x206, v22
	v_med3_i32 v27, v26, v52, v36
	v_cmp_gt_i32_sdwa s[0:1], v19, v27 src0_sel:WORD_0 src1_sel:DWORD
	v_cmp_eq_u32_sdwa s[24:25], v19, v36 src0_sel:WORD_0 src1_sel:DWORD
	v_lshl_add_u64 v[24:25], v[2:3], 1, v[38:39]
	s_and_saveexec_b64 s[28:29], s[0:1]
	global_store_short v[24:25], v16, off
	s_mov_b64 exec, s[28:29]
	v_addc_co_u32_e64 v2, vcc, 0, v2, s[0:1]
	v_addc_co_u32_e64 v26, vcc, 0, v26, s[24:25]
	v_add_u32_e32 v16, 0x207, v22
	v_med3_i32 v27, v26, v52, v36
	v_cmp_gt_i32_sdwa s[0:1], v19, v27 src0_sel:WORD_1 src1_sel:DWORD
	v_cmp_eq_u32_sdwa s[24:25], v19, v36 src0_sel:WORD_1 src1_sel:DWORD
	v_lshl_add_u64 v[18:19], v[2:3], 1, v[38:39]
	s_and_saveexec_b64 s[28:29], s[0:1]
	global_store_short v[18:19], v16, off
	s_mov_b64 exec, s[28:29]
	v_addc_co_u32_e64 v2, vcc, 0, v2, s[0:1]
	v_addc_co_u32_e64 v26, vcc, 0, v26, s[24:25]
	v_add_u32_e32 v16, 0x208, v22
	v_med3_i32 v27, v26, v52, v36
	v_cmp_gt_i32_sdwa s[0:1], v12, v27 src0_sel:WORD_0 src1_sel:DWORD
	v_cmp_eq_u32_sdwa s[24:25], v12, v36 src0_sel:WORD_0 src1_sel:DWORD
	v_lshl_add_u64 v[18:19], v[2:3], 1, v[38:39]
	s_and_saveexec_b64 s[28:29], s[0:1]
	global_store_short v[18:19], v16, off
	s_mov_b64 exec, s[28:29]
	v_addc_co_u32_e64 v2, vcc, 0, v2, s[0:1]
	v_addc_co_u32_e64 v26, vcc, 0, v26, s[24:25]
	v_add_u32_e32 v16, 0x209, v22
	v_med3_i32 v27, v26, v52, v36
	v_cmp_gt_i32_sdwa s[0:1], v12, v27 src0_sel:WORD_1 src1_sel:DWORD
	v_cmp_eq_u32_sdwa s[24:25], v12, v36 src0_sel:WORD_1 src1_sel:DWORD
	v_lshl_add_u64 v[18:19], v[2:3], 1, v[38:39]
	s_and_saveexec_b64 s[28:29], s[0:1]
	global_store_short v[18:19], v16, off
	s_mov_b64 exec, s[28:29]
	v_addc_co_u32_e64 v2, vcc, 0, v2, s[0:1]
	v_addc_co_u32_e64 v26, vcc, 0, v26, s[24:25]
	v_add_u32_e32 v16, 0x20a, v22
	v_med3_i32 v27, v26, v52, v36
	v_cmp_gt_i32_sdwa s[0:1], v13, v27 src0_sel:WORD_0 src1_sel:DWORD
	v_cmp_eq_u32_sdwa s[24:25], v13, v36 src0_sel:WORD_0 src1_sel:DWORD
	v_lshl_add_u64 v[18:19], v[2:3], 1, v[38:39]
	s_and_saveexec_b64 s[28:29], s[0:1]
	global_store_short v[18:19], v16, off
	s_mov_b64 exec, s[28:29]
	v_addc_co_u32_e64 v2, vcc, 0, v2, s[0:1]
	v_addc_co_u32_e64 v26, vcc, 0, v26, s[24:25]
	v_add_u32_e32 v16, 0x20b, v22
	v_med3_i32 v27, v26, v52, v36
	v_cmp_gt_i32_sdwa s[0:1], v13, v27 src0_sel:WORD_1 src1_sel:DWORD
	v_cmp_eq_u32_sdwa s[24:25], v13, v36 src0_sel:WORD_1 src1_sel:DWORD
	v_lshl_add_u64 v[12:13], v[2:3], 1, v[38:39]
	s_and_saveexec_b64 s[28:29], s[0:1]
	global_store_short v[12:13], v16, off
	s_mov_b64 exec, s[28:29]
	v_addc_co_u32_e64 v2, vcc, 0, v2, s[0:1]
	v_addc_co_u32_e64 v26, vcc, 0, v26, s[24:25]
	v_add_u32_e32 v12, 0x20c, v22
	v_med3_i32 v27, v26, v52, v36
	v_cmp_gt_i32_sdwa s[0:1], v14, v27 src0_sel:WORD_0 src1_sel:DWORD
	v_cmp_eq_u32_sdwa s[24:25], v14, v36 src0_sel:WORD_0 src1_sel:DWORD
	v_lshl_add_u64 v[16:17], v[2:3], 1, v[38:39]
	s_and_saveexec_b64 s[28:29], s[0:1]
	global_store_short v[16:17], v12, off
	s_mov_b64 exec, s[28:29]
	v_addc_co_u32_e64 v2, vcc, 0, v2, s[0:1]
	v_addc_co_u32_e64 v26, vcc, 0, v26, s[24:25]
	v_add_u32_e32 v12, 0x20d, v22
	v_med3_i32 v27, v26, v52, v36
	v_cmp_gt_i32_sdwa s[0:1], v14, v27 src0_sel:WORD_1 src1_sel:DWORD
	v_cmp_eq_u32_sdwa s[24:25], v14, v36 src0_sel:WORD_1 src1_sel:DWORD
	v_lshl_add_u64 v[16:17], v[2:3], 1, v[38:39]
	s_and_saveexec_b64 s[28:29], s[0:1]
	global_store_short v[16:17], v12, off
	s_mov_b64 exec, s[28:29]
	v_addc_co_u32_e64 v2, vcc, 0, v2, s[0:1]
	v_addc_co_u32_e64 v26, vcc, 0, v26, s[24:25]
	v_add_u32_e32 v12, 0x20e, v22
	v_med3_i32 v27, v26, v52, v36
	v_cmp_gt_i32_sdwa s[0:1], v15, v27 src0_sel:WORD_0 src1_sel:DWORD
	v_cmp_eq_u32_sdwa s[24:25], v15, v36 src0_sel:WORD_0 src1_sel:DWORD
	v_lshl_add_u64 v[16:17], v[2:3], 1, v[38:39]
	s_and_saveexec_b64 s[28:29], s[0:1]
	global_store_short v[16:17], v12, off
	s_mov_b64 exec, s[28:29]
	v_addc_co_u32_e64 v2, vcc, 0, v2, s[0:1]
	v_addc_co_u32_e64 v26, vcc, 0, v26, s[24:25]
	v_med3_i32 v27, v26, v52, v36
	v_cmp_gt_i32_sdwa s[24:25], v15, v27 src0_sel:WORD_1 src1_sel:DWORD
	v_lshl_add_u64 v[12:13], v[2:3], 1, v[38:39]
	v_or_b32_e32 v27, 15, v20
	s_and_saveexec_b64 s[28:29], s[24:25]
	global_store_short v[12:13], v27, off
	s_mov_b64 exec, s[28:29]

.LBB0_1104:
	ds_read_u16 v2, v50 offset:36960
	s_waitcnt lgkmcnt(0)
	v_cmp_ne_u16_e32 vcc, 0, v2
	s_and_saveexec_b64 s[18:19], vcc
	s_cbranch_execz .LBB0_710
	ds_read_u16 v2, v49 offset:36960
	s_waitcnt vmcnt(3)
	v_add_u32_e32 v12, 0x11260, v49
	ds_read_b32 v12, v12
	v_lshl_add_u64 v[14:15], v[40:41], 0, s[16:17]
	s_mov_b64 s[0:1], 0x300
	s_waitcnt lgkmcnt(1)
	v_lshrrev_b32_e32 v13, 8, v2
	v_and_b32_e32 v2, 0xff, v2
	v_cndmask_b32_e64 v13, v13, 0, s[22:23]
	v_cndmask_b32_e64 v2, v2, 0, s[22:23]
	s_waitcnt vmcnt(2) lgkmcnt(0)
	v_add_u32_sdwa v18, v13, v12 dst_sel:DWORD dst_unused:UNUSED_PAD src0_sel:DWORD src1_sel:WORD_1
	v_add_u32_sdwa v19, v2, v12 dst_sel:DWORD dst_unused:UNUSED_PAD src0_sel:DWORD src1_sel:WORD_0
	v_lshl_add_u64 v[12:13], v[14:15], 0, s[0:1]
	s_waitcnt vmcnt(0)
	v_min_i32_e32 v2, v18, v37
	v_add_u32_e32 v2, v2, v19
	v_add_u32_e32 v18, v53, v18
	v_med3_i32 v19, v18, v52, v36
	v_cmp_gt_i32_sdwa s[0:1], v8, v19 src0_sel:WORD_0 src1_sel:DWORD
	v_cmp_eq_u32_sdwa s[24:25], v8, v36 src0_sel:WORD_0 src1_sel:DWORD
	v_lshl_add_u64 v[16:17], v[2:3], 1, v[38:39]
	s_and_saveexec_b64 s[26:27], s[0:1]
	global_store_short v[16:17], v12, off
	s_mov_b64 exec, s[26:27]
	v_addc_co_u32_e64 v2, vcc, 0, v2, s[0:1]
	v_addc_co_u32_e64 v18, vcc, 0, v18, s[24:25]
	v_add_u32_e32 v16, 0x301, v14
	v_med3_i32 v19, v18, v52, v36
	v_cmp_gt_i32_sdwa s[0:1], v8, v19 src0_sel:WORD_1 src1_sel:DWORD
	v_cmp_eq_u32_sdwa s[24:25], v8, v36 src0_sel:WORD_1 src1_sel:DWORD
	v_lshl_add_u64 v[20:21], v[2:3], 1, v[38:39]
	s_and_saveexec_b64 s[26:27], s[0:1]
	global_store_short v[20:21], v16, off
	s_mov_b64 exec, s[26:27]
	v_addc_co_u32_e64 v2, vcc, 0, v2, s[0:1]
	v_addc_co_u32_e64 v18, vcc, 0, v18, s[24:25]
	v_add_u32_e32 v16, 0x302, v14
	v_med3_i32 v19, v18, v52, v36
	v_cmp_gt_i32_sdwa s[0:1], v9, v19 src0_sel:WORD_0 src1_sel:DWORD
	v_cmp_eq_u32_sdwa s[24:25], v9, v36 src0_sel:WORD_0 src1_sel:DWORD
	v_lshl_add_u64 v[20:21], v[2:3], 1, v[38:39]
	s_and_saveexec_b64 s[26:27], s[0:1]
	global_store_short v[20:21], v16, off
	s_mov_b64 exec, s[26:27]
	v_addc_co_u32_e64 v2, vcc, 0, v2, s[0:1]
	v_addc_co_u32_e64 v18, vcc, 0, v18, s[24:25]
	v_add_u32_e32 v16, 0x303, v14
	v_med3_i32 v19, v18, v52, v36
	v_cmp_gt_i32_sdwa s[0:1], v9, v19 src0_sel:WORD_1 src1_sel:DWORD
	v_cmp_eq_u32_sdwa s[24:25], v9, v36 src0_sel:WORD_1 src1_sel:DWORD
	v_lshl_add_u64 v[8:9], v[2:3], 1, v[38:39]
	s_and_saveexec_b64 s[26:27], s[0:1]
	global_store_short v[8:9], v16, off
	s_mov_b64 exec, s[26:27]
	v_addc_co_u32_e64 v2, vcc, 0, v2, s[0:1]
	v_addc_co_u32_e64 v18, vcc, 0, v18, s[24:25]
	v_add_u32_e32 v8, 0x304, v14
	v_med3_i32 v19, v18, v52, v36
	v_cmp_gt_i32_sdwa s[0:1], v10, v19 src0_sel:WORD_0 src1_sel:DWORD
	v_cmp_eq_u32_sdwa s[24:25], v10, v36 src0_sel:WORD_0 src1_sel:DWORD
	v_lshl_add_u64 v[16:17], v[2:3], 1, v[38:39]
	s_and_saveexec_b64 s[26:27], s[0:1]
	global_store_short v[16:17], v8, off
	s_mov_b64 exec, s[26:27]
	v_addc_co_u32_e64 v2, vcc, 0, v2, s[0:1]
	v_addc_co_u32_e64 v18, vcc, 0, v18, s[24:25]
	v_add_u32_e32 v8, 0x305, v14
	v_med3_i32 v19, v18, v52, v36
	v_cmp_gt_i32_sdwa s[0:1], v10, v19 src0_sel:WORD_1 src1_sel:DWORD
	v_cmp_eq_u32_sdwa s[24:25], v10, v36 src0_sel:WORD_1 src1_sel:DWORD
	v_lshl_add_u64 v[16:17], v[2:3], 1, v[38:39]
	s_and_saveexec_b64 s[26:27], s[0:1]
	global_store_short v[16:17], v8, off
	s_mov_b64 exec, s[26:27]
	v_addc_co_u32_e64 v2, vcc, 0, v2, s[0:1]
	v_addc_co_u32_e64 v18, vcc, 0, v18, s[24:25]
	v_add_u32_e32 v8, 0x306, v14
	v_med3_i32 v19, v18, v52, v36
	v_cmp_gt_i32_sdwa s[0:1], v11, v19 src0_sel:WORD_0 src1_sel:DWORD
	v_cmp_eq_u32_sdwa s[24:25], v11, v36 src0_sel:WORD_0 src1_sel:DWORD
	v_lshl_add_u64 v[16:17], v[2:3], 1, v[38:39]
	s_and_saveexec_b64 s[26:27], s[0:1]
	global_store_short v[16:17], v8, off
	s_mov_b64 exec, s[26:27]
	v_addc_co_u32_e64 v2, vcc, 0, v2, s[0:1]
	v_addc_co_u32_e64 v18, vcc, 0, v18, s[24:25]
	v_add_u32_e32 v8, 0x307, v14
	v_med3_i32 v19, v18, v52, v36
	v_cmp_gt_i32_sdwa s[0:1], v11, v19 src0_sel:WORD_1 src1_sel:DWORD
	v_cmp_eq_u32_sdwa s[24:25], v11, v36 src0_sel:WORD_1 src1_sel:DWORD
	v_lshl_add_u64 v[10:11], v[2:3], 1, v[38:39]
	s_and_saveexec_b64 s[26:27], s[0:1]
	global_store_short v[10:11], v8, off
	s_mov_b64 exec, s[26:27]
	v_addc_co_u32_e64 v2, vcc, 0, v2, s[0:1]
	v_addc_co_u32_e64 v18, vcc, 0, v18, s[24:25]
	v_add_u32_e32 v8, 0x308, v14
	v_med3_i32 v19, v18, v52, v36
	v_cmp_gt_i32_sdwa s[0:1], v4, v19 src0_sel:WORD_0 src1_sel:DWORD
	v_cmp_eq_u32_sdwa s[24:25], v4, v36 src0_sel:WORD_0 src1_sel:DWORD
	v_lshl_add_u64 v[10:11], v[2:3], 1, v[38:39]
	s_and_saveexec_b64 s[26:27], s[0:1]
	global_store_short v[10:11], v8, off
	s_mov_b64 exec, s[26:27]
	v_addc_co_u32_e64 v2, vcc, 0, v2, s[0:1]
	v_addc_co_u32_e64 v18, vcc, 0, v18, s[24:25]
	v_add_u32_e32 v8, 0x309, v14
	v_med3_i32 v19, v18, v52, v36
	v_cmp_gt_i32_sdwa s[0:1], v4, v19 src0_sel:WORD_1 src1_sel:DWORD
	v_cmp_eq_u32_sdwa s[24:25], v4, v36 src0_sel:WORD_1 src1_sel:DWORD
	v_lshl_add_u64 v[10:11], v[2:3], 1, v[38:39]
	s_and_saveexec_b64 s[26:27], s[0:1]
	global_store_short v[10:11], v8, off
	s_mov_b64 exec, s[26:27]
	v_addc_co_u32_e64 v2, vcc, 0, v2, s[0:1]
	v_addc_co_u32_e64 v18, vcc, 0, v18, s[24:25]
	v_add_u32_e32 v8, 0x30a, v14
	v_med3_i32 v19, v18, v52, v36
	v_cmp_gt_i32_sdwa s[0:1], v5, v19 src0_sel:WORD_0 src1_sel:DWORD
	v_cmp_eq_u32_sdwa s[24:25], v5, v36 src0_sel:WORD_0 src1_sel:DWORD
	v_lshl_add_u64 v[10:11], v[2:3], 1, v[38:39]
	s_and_saveexec_b64 s[26:27], s[0:1]
	global_store_short v[10:11], v8, off
	s_mov_b64 exec, s[26:27]
	v_addc_co_u32_e64 v2, vcc, 0, v2, s[0:1]
	v_addc_co_u32_e64 v18, vcc, 0, v18, s[24:25]
	v_add_u32_e32 v8, 0x30b, v14
	v_med3_i32 v19, v18, v52, v36
	v_cmp_gt_i32_sdwa s[0:1], v5, v19 src0_sel:WORD_1 src1_sel:DWORD
	v_cmp_eq_u32_sdwa s[24:25], v5, v36 src0_sel:WORD_1 src1_sel:DWORD
	v_lshl_add_u64 v[4:5], v[2:3], 1, v[38:39]
	s_and_saveexec_b64 s[26:27], s[0:1]
	global_store_short v[4:5], v8, off
	s_mov_b64 exec, s[26:27]
	v_addc_co_u32_e64 v2, vcc, 0, v2, s[0:1]
	v_addc_co_u32_e64 v18, vcc, 0, v18, s[24:25]
	v_add_u32_e32 v4, 0x30c, v14
	v_med3_i32 v19, v18, v52, v36
	v_cmp_gt_i32_sdwa s[0:1], v6, v19 src0_sel:WORD_0 src1_sel:DWORD
	v_cmp_eq_u32_sdwa s[24:25], v6, v36 src0_sel:WORD_0 src1_sel:DWORD
	v_lshl_add_u64 v[8:9], v[2:3], 1, v[38:39]
	s_and_saveexec_b64 s[26:27], s[0:1]
	global_store_short v[8:9], v4, off
	s_mov_b64 exec, s[26:27]
	v_addc_co_u32_e64 v2, vcc, 0, v2, s[0:1]
	v_addc_co_u32_e64 v18, vcc, 0, v18, s[24:25]
	v_add_u32_e32 v4, 0x30d, v14
	v_med3_i32 v19, v18, v52, v36
	v_cmp_gt_i32_sdwa s[0:1], v6, v19 src0_sel:WORD_1 src1_sel:DWORD
	v_cmp_eq_u32_sdwa s[24:25], v6, v36 src0_sel:WORD_1 src1_sel:DWORD
	v_lshl_add_u64 v[8:9], v[2:3], 1, v[38:39]
	s_and_saveexec_b64 s[26:27], s[0:1]
	global_store_short v[8:9], v4, off
	s_mov_b64 exec, s[26:27]
	v_addc_co_u32_e64 v2, vcc, 0, v2, s[0:1]
	v_addc_co_u32_e64 v18, vcc, 0, v18, s[24:25]
	v_add_u32_e32 v4, 0x30e, v14
	v_med3_i32 v19, v18, v52, v36
	v_cmp_gt_i32_sdwa s[0:1], v7, v19 src0_sel:WORD_0 src1_sel:DWORD
	v_cmp_eq_u32_sdwa s[24:25], v7, v36 src0_sel:WORD_0 src1_sel:DWORD
	v_lshl_add_u64 v[8:9], v[2:3], 1, v[38:39]
	s_and_saveexec_b64 s[26:27], s[0:1]
	global_store_short v[8:9], v4, off
	s_mov_b64 exec, s[26:27]
	v_addc_co_u32_e64 v2, vcc, 0, v2, s[0:1]
	v_addc_co_u32_e64 v18, vcc, 0, v18, s[24:25]
	v_med3_i32 v19, v18, v52, v36
	v_cmp_gt_i32_sdwa s[0:1], v7, v19 src0_sel:WORD_1 src1_sel:DWORD
	v_lshl_add_u64 v[8:9], v[2:3], 1, v[38:39]
	v_or_b32_e32 v19, 15, v12
	s_and_saveexec_b64 s[26:27], s[0:1]
	global_store_short v[8:9], v19, off
	s_branch .LBB0_710
.LBB0_1229:
.LBB0_1230:
	s_andn2_saveexec_b64 s[30:31], s[30:31]
	s_cbranch_execz .LBB0_843
